# v058 with fold padded (unreachable s_nops) so fused kernel keeps the v048 code address: isolates code-placement effect
# speedup vs baseline: 1.0015x; 1.0015x over previous
.LBB1_75:
	s_endpgm
	s_nop 0
	s_nop 0
	s_nop 0
	s_nop 0
	s_nop 0
	s_nop 0
	s_nop 0
	s_nop 0
	s_nop 0
	s_nop 0
	s_nop 0
	s_nop 0
	s_nop 0
	s_nop 0
	s_nop 0
	s_nop 0
	s_nop 0
	s_nop 0
	s_nop 0
	s_nop 0
	s_nop 0
	s_nop 0
	s_nop 0
	s_nop 0
	s_nop 0
	s_nop 0
	s_nop 0
	s_nop 0
	s_nop 0
	s_nop 0
	s_nop 0
	s_nop 0
	s_nop 0
	s_nop 0
	s_nop 0
	s_nop 0
	s_nop 0
	s_nop 0
	s_nop 0
	s_nop 0
	s_nop 0
	s_nop 0
	s_nop 0
	s_nop 0
	s_nop 0
	s_nop 0
	s_nop 0
	s_nop 0
	s_nop 0
	s_nop 0
	s_nop 0
	s_nop 0
	s_nop 0
	s_nop 0
	s_nop 0
	s_nop 0
	s_nop 0
	s_nop 0
	s_nop 0
	s_nop 0
	s_nop 0
	s_nop 0
	s_nop 0
	s_nop 0
	s_nop 0
	s_nop 0
	s_nop 0
	s_nop 0
	s_nop 0
	s_nop 0
	s_nop 0
	s_nop 0
	s_nop 0
	s_nop 0
	s_nop 0
	s_nop 0
	s_nop 0
	s_nop 0
	s_nop 0
	s_nop 0
	s_nop 0
	s_nop 0
	s_nop 0
	s_nop 0
	s_nop 0
	s_nop 0
	s_nop 0
	s_nop 0
	s_nop 0
	s_nop 0
	s_nop 0
	s_nop 0
	s_nop 0
	s_nop 0
	s_nop 0
	s_nop 0
	s_nop 0
	s_nop 0
	s_nop 0
	s_nop 0
	s_nop 0
	s_nop 0
	s_nop 0
	s_nop 0
	s_nop 0
	s_nop 0
	s_nop 0
	s_nop 0
	s_nop 0
	s_nop 0
	s_nop 0
	s_nop 0
	s_nop 0
	s_nop 0
	s_nop 0
	s_nop 0
	s_nop 0
	s_nop 0
	s_nop 0
	s_nop 0
	s_nop 0
	s_nop 0
	s_nop 0
	s_nop 0
	s_nop 0
	s_nop 0
	s_nop 0
	s_nop 0
	s_nop 0
	s_nop 0
	s_nop 0
	s_nop 0
	s_nop 0
	s_nop 0
	s_nop 0
	s_nop 0
	s_nop 0
	s_nop 0
	s_nop 0
	s_nop 0
	s_nop 0
	s_nop 0
	s_nop 0
	s_nop 0
	s_nop 0
	s_nop 0
	s_nop 0
	s_nop 0
	s_nop 0
	s_nop 0
	s_nop 0
	s_nop 0
	s_nop 0
	s_nop 0
	s_nop 0
	s_nop 0
	s_nop 0
	s_nop 0
	s_nop 0
	s_nop 0
	s_nop 0
	s_nop 0
	s_nop 0
	s_nop 0
	s_nop 0
	s_nop 0
	s_nop 0
	s_nop 0
	s_nop 0
	s_nop 0
	s_nop 0
	s_nop 0
	s_nop 0
	s_nop 0
	s_nop 0
	s_nop 0
	s_nop 0
	s_nop 0
	s_nop 0
	s_nop 0
	s_nop 0
	s_nop 0
	s_nop 0
	s_nop 0
	s_nop 0
	s_nop 0
	s_nop 0
	s_nop 0
	s_nop 0
	s_nop 0
	s_nop 0
	s_nop 0
